# grid barrier: invalidate issued at arrival instead of after release, leader invalidates right after its L2 writeback, non-leaders poll the cross-XCD generation directly
# speedup vs baseline: 1.0223x; 1.0036x over previous
; __device__ __forceinline__ unsigned xb_ld(unsigned* p)              { return __hip_atomic_load(p, __ATOMIC_RELAXED, __HIP_MEMORY_SCOPE_AGENT); }
; __device__ __forceinline__ unsigned xb_add(unsigned* p, unsigned v) { return __hip_atomic_fetch_add(p, v, __ATOMIC_RELAXED, __HIP_MEMORY_SCOPE_AGENT); }
; #define XB_SPIN(cond, bar) do { unsigned _sp = 0; while (cond) { __builtin_amdgcn_s_sleep(1); \
;     if ((++_sp & 255u) == 0u) { if (xb_ld(&(bar)[XB_TMO])) break; if (_sp > XB_SPIN_CAP) { atomicAdd(&(bar)[XB_TMO], 1u); break; } } } } while (0)
; __device__ __forceinline__ void xcd_barrier(const XcdBarrier& b, int tid  ) {
;     asm volatile("s_waitcnt vmcnt(0)" ::: "memory");
;     __syncthreads();
;     if (tid == 0) {
;         unsigned* bar = b.bar; unsigned xq = b.x; asm volatile("" : "+s"(xq));
;         __builtin_amdgcn_s_waitcnt(0);
;         unsigned nloc = b.st[0], nx = b.st[1];
;         if (nloc == 0u) { xcd_barrier_complete(bar, xq, nloc, nx); b.st[0] = nloc; b.st[1] = nx; }
;         const unsigned old = xb_add(&bar[XB_XSUB(xq)], 1u);
;         const unsigned gen = old / nloc;
;         if (old + 1u == (gen + 1u) * nloc) {
;             __builtin_amdgcn_fence(__ATOMIC_RELEASE, "agent");
;             asm volatile("s_waitcnt vmcnt(0)" ::: "memory");
;             const unsigned og = xb_add(&bar[XB_TOP], 1u);
;             const unsigned tg = og / nx;
;             if (og + 1u == (tg + 1u) * nx) xb_add(&bar[XB_TOPGEN], 1u);
;             else XB_SPIN(xb_ld(&bar[XB_TOPGEN]) == tg, bar);
;             __builtin_amdgcn_fence(__ATOMIC_ACQUIRE, "agent");
;             xb_add(&bar[XB_XGEN(xq)], 1u);
;             asm volatile("s_waitcnt vmcnt(0)" ::: "memory");
;         } else {
;             XB_SPIN(xb_ld(&bar[XB_XGEN(xq)]) == gen, bar);
.LBB0_92:
	s_or_b64 exec, exec, s[4:5]
	v_cvt_f32_u32_e32 v4, v2
	s_waitcnt vmcnt(0)
	v_readfirstlane_b32 s0, v3
	v_sub_u32_e32 v3, 0, v2
	v_rcp_iflag_f32_e32 v4, v4
	v_add_u32_e32 v5, s0, v1
	v_mul_f32_e32 v4, 0x4f7ffffe, v4
	v_cvt_u32_f32_e32 v4, v4
	v_mul_lo_u32 v1, v3, v4
	v_mul_hi_u32 v1, v4, v1
	v_add_u32_e32 v1, v4, v1
	v_mul_hi_u32 v1, v5, v1
	v_mul_lo_u32 v3, v1, v2
	v_sub_u32_e32 v3, v5, v3
	v_add_u32_e32 v4, 1, v1
	v_cmp_ge_u32_e32 vcc, v3, v2
	s_nop 1
	v_cndmask_b32_e32 v1, v1, v4, vcc
	v_sub_u32_e32 v4, v3, v2
	v_cndmask_b32_e32 v3, v3, v4, vcc
	v_add_u32_e32 v4, 1, v1
	v_cmp_ge_u32_e32 vcc, v3, v2
	v_add_u32_e32 v3, 1, v5
	s_nop 0
	v_cndmask_b32_e32 v1, v1, v4, vcc
	v_mul_lo_u32 v4, v2, v1
	v_add_u32_e32 v2, v4, v2
	v_cmp_ne_u32_e32 vcc, v3, v2
	s_and_saveexec_b64 s[0:1], vcc
	s_xor_b64 s[0:1], exec, s[0:1]
	s_cbranch_execz .LBB0_106
	buffer_inv sc1
	s_movk_i32 s4, 0xd40
	s_mov_b32 s5, 0
	s_lshl_b64 s[4:5], s[4:5], 2
	s_add_u32 s6, s64, s4
	s_addc_u32 s7, s65, s5
	s_waitcnt lgkmcnt(0)
	v_mov_b32_e32 v0, 0
	global_load_dword v2, v0, s[6:7] sc1
	s_waitcnt vmcnt(0)
	v_cmp_eq_u32_e32 vcc, v2, v1
	s_and_saveexec_b64 s[4:5], vcc
	s_cbranch_execz .LBB0_105
	s_mov_b32 s18, 1
	s_mov_b64 s[8:9], 0
	s_branch .LBB0_96

; __device__ __forceinline__ unsigned xb_ld(unsigned* p)              { return __hip_atomic_load(p, __ATOMIC_RELAXED, __HIP_MEMORY_SCOPE_AGENT); }
; __device__ __forceinline__ unsigned xb_add(unsigned* p, unsigned v) { return __hip_atomic_fetch_add(p, v, __ATOMIC_RELAXED, __HIP_MEMORY_SCOPE_AGENT); }
; #define XB_SPIN(cond, bar) do { unsigned _sp = 0; while (cond) { __builtin_amdgcn_s_sleep(1); \
;     if ((++_sp & 255u) == 0u) { if (xb_ld(&(bar)[XB_TMO])) break; if (_sp > XB_SPIN_CAP) { atomicAdd(&(bar)[XB_TMO], 1u); break; } } } } while (0)
; __device__ __forceinline__ void xcd_barrier(const XcdBarrier& b, int tid  ) {
;     ...
;         if (old + 1u == (gen + 1u) * nloc) {
;             __builtin_amdgcn_fence(__ATOMIC_RELEASE, "agent");
;             asm volatile("s_waitcnt vmcnt(0)" ::: "memory");
;             const unsigned og = xb_add(&bar[XB_TOP], 1u);
;             const unsigned tg = og / nx;
;             if (og + 1u == (tg + 1u) * nx) xb_add(&bar[XB_TOPGEN], 1u);
;             else XB_SPIN(xb_ld(&bar[XB_TOPGEN]) == tg, bar);
;             __builtin_amdgcn_fence(__ATOMIC_ACQUIRE, "agent");
;             xb_add(&bar[XB_XGEN(xq)], 1u);
;             asm volatile("s_waitcnt vmcnt(0)" ::: "memory");
;         } else {
;             XB_SPIN(xb_ld(&bar[XB_XGEN(xq)]) == gen, bar);
;             __builtin_amdgcn_fence(__ATOMIC_ACQUIRE, "agent");
;             asm volatile("s_waitcnt vmcnt(0)" ::: "memory");
.LBB0_105:
	s_or_b64 exec, exec, s[4:5]
	s_waitcnt vmcnt(0)
	s_waitcnt vmcnt(0)
.LBB0_106:
	s_andn2_saveexec_b64 s[0:1], s[0:1]
	s_cbranch_execz .LBB0_126
	s_mov_b64 s[0:1], exec
	buffer_wbl2 sc1
	s_waitcnt lgkmcnt(0)
	s_waitcnt vmcnt(0)
	buffer_inv sc1
	s_waitcnt vmcnt(0)
	v_mbcnt_lo_u32_b32 v1, s0, 0
	v_mbcnt_hi_u32_b32 v1, s1, v1
	v_cmp_eq_u32_e32 vcc, 0, v1
	s_and_saveexec_b64 s[4:5], vcc
	s_cbranch_execz .LBB0_109
	s_bcnt1_i32_b64 s0, s[0:1]
	v_mov_b32_e32 v2, 0x3000
	v_mov_b32_e32 v3, s0
	global_atomic_add v2, v2, v3, s[64:65] offset:1024 sc0

; __device__ __forceinline__ unsigned xb_ld(unsigned* p)              { return __hip_atomic_load(p, __ATOMIC_RELAXED, __HIP_MEMORY_SCOPE_AGENT); }
; __device__ __forceinline__ unsigned xb_add(unsigned* p, unsigned v) { return __hip_atomic_fetch_add(p, v, __ATOMIC_RELAXED, __HIP_MEMORY_SCOPE_AGENT); }
; #define XB_SPIN(cond, bar) do { unsigned _sp = 0; while (cond) { __builtin_amdgcn_s_sleep(1); \
;     if ((++_sp & 255u) == 0u) { if (xb_ld(&(bar)[XB_TMO])) break; if (_sp > XB_SPIN_CAP) { atomicAdd(&(bar)[XB_TMO], 1u); break; } } } } while (0)
; __device__ __forceinline__ void xcd_barrier(const XcdBarrier& b, int tid  ) {
;     ...
;             else XB_SPIN(xb_ld(&bar[XB_TOPGEN]) == tg, bar);
;             __builtin_amdgcn_fence(__ATOMIC_ACQUIRE, "agent");
;             xb_add(&bar[XB_XGEN(xq)], 1u);
;             asm volatile("s_waitcnt vmcnt(0)" ::: "memory");
.LBB0_123:
	s_or_b64 exec, exec, s[0:1]
	s_mov_b64 s[0:1], exec
	v_mbcnt_lo_u32_b32 v0, s0, 0
	v_mbcnt_hi_u32_b32 v0, s1, v0
	s_mov_b32 s7, 0
	v_cmp_eq_u32_e32 vcc, 0, v0
	s_waitcnt vmcnt(0)
	s_and_saveexec_b64 s[4:5], vcc
	s_cbranch_execz .LBB0_125
	s_add_i32 s6, s21, 0x900
	s_lshl_b64 s[6:7], s[6:7], 2
	s_add_u32 s6, s64, s6
	s_addc_u32 s7, s65, s7
	s_bcnt1_i32_b64 s0, s[0:1]
	v_mov_b32_e32 v0, 0
	v_mov_b32_e32 v1, s0
	global_atomic_add v0, v1, s[6:7]

; __device__ __forceinline__ unsigned xb_ld(unsigned* p)              { return __hip_atomic_load(p, __ATOMIC_RELAXED, __HIP_MEMORY_SCOPE_AGENT); }
; __device__ __forceinline__ unsigned xb_add(unsigned* p, unsigned v) { return __hip_atomic_fetch_add(p, v, __ATOMIC_RELAXED, __HIP_MEMORY_SCOPE_AGENT); }
; #define XB_SPIN(cond, bar) do { unsigned _sp = 0; while (cond) { __builtin_amdgcn_s_sleep(1); \
;     if ((++_sp & 255u) == 0u) { if (xb_ld(&(bar)[XB_TMO])) break; if (_sp > XB_SPIN_CAP) { atomicAdd(&(bar)[XB_TMO], 1u); break; } } } } while (0)
; __device__ __forceinline__ void xcd_barrier(const XcdBarrier& b, int tid  ) {
;     asm volatile("s_waitcnt vmcnt(0)" ::: "memory");
;     __syncthreads();
;     if (tid == 0) {
;         unsigned* bar = b.bar; unsigned xq = b.x; asm volatile("" : "+s"(xq));
;         __builtin_amdgcn_s_waitcnt(0);
;         unsigned nloc = b.st[0], nx = b.st[1];
;         if (nloc == 0u) { xcd_barrier_complete(bar, xq, nloc, nx); b.st[0] = nloc; b.st[1] = nx; }
;         const unsigned old = xb_add(&bar[XB_XSUB(xq)], 1u);
;         const unsigned gen = old / nloc;
;         if (old + 1u == (gen + 1u) * nloc) {
;             __builtin_amdgcn_fence(__ATOMIC_RELEASE, "agent");
;             asm volatile("s_waitcnt vmcnt(0)" ::: "memory");
;             const unsigned og = xb_add(&bar[XB_TOP], 1u);
;             const unsigned tg = og / nx;
;             if (og + 1u == (tg + 1u) * nx) xb_add(&bar[XB_TOPGEN], 1u);
;             else XB_SPIN(xb_ld(&bar[XB_TOPGEN]) == tg, bar);
;             __builtin_amdgcn_fence(__ATOMIC_ACQUIRE, "agent");
;             xb_add(&bar[XB_XGEN(xq)], 1u);
;             asm volatile("s_waitcnt vmcnt(0)" ::: "memory");
;         } else {
;             XB_SPIN(xb_ld(&bar[XB_XGEN(xq)]) == gen, bar);
.LBB0_184:
	s_or_b64 exec, exec, s[4:5]
	v_cvt_f32_u32_e32 v4, v2
	s_waitcnt vmcnt(0)
	v_readfirstlane_b32 s0, v3
	v_sub_u32_e32 v3, 0, v2
	v_rcp_iflag_f32_e32 v4, v4
	v_add_u32_e32 v5, s0, v1
	v_mul_f32_e32 v4, 0x4f7ffffe, v4
	v_cvt_u32_f32_e32 v4, v4
	v_mul_lo_u32 v1, v3, v4
	v_mul_hi_u32 v1, v4, v1
	v_add_u32_e32 v1, v4, v1
	v_mul_hi_u32 v1, v5, v1
	v_mul_lo_u32 v3, v1, v2
	v_sub_u32_e32 v3, v5, v3
	v_add_u32_e32 v4, 1, v1
	v_cmp_ge_u32_e32 vcc, v3, v2
	s_nop 1
	v_cndmask_b32_e32 v1, v1, v4, vcc
	v_sub_u32_e32 v4, v3, v2
	v_cndmask_b32_e32 v3, v3, v4, vcc
	v_add_u32_e32 v4, 1, v1
	v_cmp_ge_u32_e32 vcc, v3, v2
	v_add_u32_e32 v3, 1, v5
	s_nop 0
	v_cndmask_b32_e32 v1, v1, v4, vcc
	v_mul_lo_u32 v4, v2, v1
	v_add_u32_e32 v2, v4, v2
	v_cmp_ne_u32_e32 vcc, v3, v2
	s_and_saveexec_b64 s[0:1], vcc
	s_xor_b64 s[0:1], exec, s[0:1]
	s_cbranch_execz .LBB0_198
	buffer_inv sc1
	s_movk_i32 s62, 0xd40
	s_lshl_b64 s[4:5], s[62:63], 2
	s_add_u32 s6, s64, s4
	s_addc_u32 s7, s65, s5
	s_waitcnt lgkmcnt(0)
	global_load_dword v0, v81, s[6:7] sc1
	s_waitcnt vmcnt(0)
	v_cmp_eq_u32_e32 vcc, v0, v1
	s_and_saveexec_b64 s[4:5], vcc
	s_cbranch_execz .LBB0_197
	s_mov_b32 s20, 1
	s_mov_b64 s[8:9], 0
	s_branch .LBB0_188

; __device__ __forceinline__ unsigned xb_add(unsigned* p, unsigned v) { return __hip_atomic_fetch_add(p, v, __ATOMIC_RELAXED, __HIP_MEMORY_SCOPE_AGENT); }
; __device__ __forceinline__ void xcd_barrier(const XcdBarrier& b, int tid  ) {
;     ...
;         if (old + 1u == (gen + 1u) * nloc) {
;             __builtin_amdgcn_fence(__ATOMIC_RELEASE, "agent");
;             asm volatile("s_waitcnt vmcnt(0)" ::: "memory");
;             const unsigned og = xb_add(&bar[XB_TOP], 1u);
;             const unsigned tg = og / nx;
;             if (og + 1u == (tg + 1u) * nx) xb_add(&bar[XB_TOPGEN], 1u);
.LBB0_198:
	s_andn2_saveexec_b64 s[0:1], s[0:1]
	s_cbranch_execz .LBB0_218
	s_mov_b64 s[0:1], exec
	buffer_wbl2 sc1
	s_waitcnt lgkmcnt(0)
	s_waitcnt vmcnt(0)
	buffer_inv sc1
	s_waitcnt vmcnt(0)
	v_mbcnt_lo_u32_b32 v1, s0, 0
	v_mbcnt_hi_u32_b32 v1, s1, v1
	v_cmp_eq_u32_e32 vcc, 0, v1
	s_and_saveexec_b64 s[4:5], vcc
	s_cbranch_execz .LBB0_201
	s_bcnt1_i32_b64 s0, s[0:1]
	v_mov_b32_e32 v2, s0
	v_readlane_b32 s0, v254, 17
	v_readlane_b32 s1, v254, 18
	s_nop 4
	global_atomic_add v2, v81, v2, s[0:1] sc0

; __device__ __forceinline__ unsigned xb_ld(unsigned* p)              { return __hip_atomic_load(p, __ATOMIC_RELAXED, __HIP_MEMORY_SCOPE_AGENT); }
; __device__ __forceinline__ unsigned xb_add(unsigned* p, unsigned v) { return __hip_atomic_fetch_add(p, v, __ATOMIC_RELAXED, __HIP_MEMORY_SCOPE_AGENT); }
; #define XB_SPIN(cond, bar) do { unsigned _sp = 0; while (cond) { __builtin_amdgcn_s_sleep(1); \
;     if ((++_sp & 255u) == 0u) { if (xb_ld(&(bar)[XB_TMO])) break; if (_sp > XB_SPIN_CAP) { atomicAdd(&(bar)[XB_TMO], 1u); break; } } } } while (0)
; __device__ __forceinline__ void xcd_barrier(const XcdBarrier& b, int tid  ) {
;     ...
;             else XB_SPIN(xb_ld(&bar[XB_TOPGEN]) == tg, bar);
;             __builtin_amdgcn_fence(__ATOMIC_ACQUIRE, "agent");
;             xb_add(&bar[XB_XGEN(xq)], 1u);
;             asm volatile("s_waitcnt vmcnt(0)" ::: "memory");
.LBB0_215:
	s_or_b64 exec, exec, s[0:1]
	s_mov_b64 s[0:1], exec
	v_mbcnt_lo_u32_b32 v0, s0, 0
	v_mbcnt_hi_u32_b32 v0, s1, v0
	v_cmp_eq_u32_e32 vcc, 0, v0
	s_waitcnt vmcnt(0)
	s_and_saveexec_b64 s[4:5], vcc
	s_cbranch_execz .LBB0_217
	s_add_i32 s62, s19, 0x900
	s_lshl_b64 s[6:7], s[62:63], 2
	s_add_u32 s6, s64, s6
	s_addc_u32 s7, s65, s7
	s_bcnt1_i32_b64 s0, s[0:1]
	v_mov_b32_e32 v0, s0
	global_atomic_add v81, v0, s[6:7]

; __device__ __forceinline__ unsigned xb_ld(unsigned* p)              { return __hip_atomic_load(p, __ATOMIC_RELAXED, __HIP_MEMORY_SCOPE_AGENT); }
; __device__ __forceinline__ unsigned xb_add(unsigned* p, unsigned v) { return __hip_atomic_fetch_add(p, v, __ATOMIC_RELAXED, __HIP_MEMORY_SCOPE_AGENT); }
; #define XB_SPIN(cond, bar) do { unsigned _sp = 0; while (cond) { __builtin_amdgcn_s_sleep(1); \
;     if ((++_sp & 255u) == 0u) { if (xb_ld(&(bar)[XB_TMO])) break; if (_sp > XB_SPIN_CAP) { atomicAdd(&(bar)[XB_TMO], 1u); break; } } } } while (0)
; __device__ __forceinline__ void xcd_barrier(const XcdBarrier& b, int tid  ) {
;     asm volatile("s_waitcnt vmcnt(0)" ::: "memory");
;     __syncthreads();
;     if (tid == 0) {
;         unsigned* bar = b.bar; unsigned xq = b.x; asm volatile("" : "+s"(xq));
;         __builtin_amdgcn_s_waitcnt(0);
;         unsigned nloc = b.st[0], nx = b.st[1];
;         if (nloc == 0u) { xcd_barrier_complete(bar, xq, nloc, nx); b.st[0] = nloc; b.st[1] = nx; }
;         const unsigned old = xb_add(&bar[XB_XSUB(xq)], 1u);
;         const unsigned gen = old / nloc;
;         if (old + 1u == (gen + 1u) * nloc) {
;             __builtin_amdgcn_fence(__ATOMIC_RELEASE, "agent");
;             asm volatile("s_waitcnt vmcnt(0)" ::: "memory");
;             const unsigned og = xb_add(&bar[XB_TOP], 1u);
;             const unsigned tg = og / nx;
;             if (og + 1u == (tg + 1u) * nx) xb_add(&bar[XB_TOPGEN], 1u);
;             else XB_SPIN(xb_ld(&bar[XB_TOPGEN]) == tg, bar);
;             __builtin_amdgcn_fence(__ATOMIC_ACQUIRE, "agent");
;             xb_add(&bar[XB_XGEN(xq)], 1u);
;             asm volatile("s_waitcnt vmcnt(0)" ::: "memory");
;         } else {
;             XB_SPIN(xb_ld(&bar[XB_XGEN(xq)]) == gen, bar);
.LBB0_992:
	s_or_b64 exec, exec, s[6:7]
	v_cvt_f32_u32_e32 v4, v2
	s_waitcnt vmcnt(0)
	v_readfirstlane_b32 s0, v3
	v_sub_u32_e32 v3, 0, v2
	v_rcp_iflag_f32_e32 v4, v4
	v_add_u32_e32 v5, s0, v1
	v_mul_f32_e32 v4, 0x4f7ffffe, v4
	v_cvt_u32_f32_e32 v4, v4
	v_mul_lo_u32 v1, v3, v4
	v_mul_hi_u32 v1, v4, v1
	v_add_u32_e32 v1, v4, v1
	v_mul_hi_u32 v1, v5, v1
	v_mul_lo_u32 v3, v1, v2
	v_sub_u32_e32 v3, v5, v3
	v_add_u32_e32 v4, 1, v1
	v_cmp_ge_u32_e32 vcc, v3, v2
	s_nop 1
	v_cndmask_b32_e32 v1, v1, v4, vcc
	v_sub_u32_e32 v4, v3, v2
	v_cndmask_b32_e32 v3, v3, v4, vcc
	v_add_u32_e32 v4, 1, v1
	v_cmp_ge_u32_e32 vcc, v3, v2
	v_add_u32_e32 v3, 1, v5
	s_nop 0
	v_cndmask_b32_e32 v1, v1, v4, vcc
	v_mul_lo_u32 v4, v2, v1
	v_add_u32_e32 v2, v4, v2
	v_cmp_ne_u32_e32 vcc, v3, v2
	s_and_saveexec_b64 s[0:1], vcc
	s_xor_b64 s[0:1], exec, s[0:1]
	s_cbranch_execz .LBB0_1006
	buffer_inv sc1
	s_movk_i32 s62, 0xd40
	s_lshl_b64 s[6:7], s[62:63], 2
	s_add_u32 s8, s64, s6
	s_addc_u32 s9, s65, s7
	s_waitcnt lgkmcnt(0)
	global_load_dword v0, v81, s[8:9] sc1
	s_waitcnt vmcnt(0)
	v_cmp_eq_u32_e32 vcc, v0, v1
	s_and_saveexec_b64 s[6:7], vcc
	s_cbranch_execz .LBB0_1005
	s_mov_b32 s22, 1
	s_mov_b64 s[10:11], 0
	s_branch .LBB0_996

; __device__ __forceinline__ unsigned xb_ld(unsigned* p)              { return __hip_atomic_load(p, __ATOMIC_RELAXED, __HIP_MEMORY_SCOPE_AGENT); }
; __device__ __forceinline__ unsigned xb_add(unsigned* p, unsigned v) { return __hip_atomic_fetch_add(p, v, __ATOMIC_RELAXED, __HIP_MEMORY_SCOPE_AGENT); }
; #define XB_SPIN(cond, bar) do { unsigned _sp = 0; while (cond) { __builtin_amdgcn_s_sleep(1); \
;     if ((++_sp & 255u) == 0u) { if (xb_ld(&(bar)[XB_TMO])) break; if (_sp > XB_SPIN_CAP) { atomicAdd(&(bar)[XB_TMO], 1u); break; } } } } while (0)
; __device__ __forceinline__ void xcd_barrier(const XcdBarrier& b, int tid  ) {
;     ...
;         if (old + 1u == (gen + 1u) * nloc) {
;             __builtin_amdgcn_fence(__ATOMIC_RELEASE, "agent");
;             asm volatile("s_waitcnt vmcnt(0)" ::: "memory");
;             const unsigned og = xb_add(&bar[XB_TOP], 1u);
;             const unsigned tg = og / nx;
;             if (og + 1u == (tg + 1u) * nx) xb_add(&bar[XB_TOPGEN], 1u);
;             else XB_SPIN(xb_ld(&bar[XB_TOPGEN]) == tg, bar);
;             __builtin_amdgcn_fence(__ATOMIC_ACQUIRE, "agent");
;             xb_add(&bar[XB_XGEN(xq)], 1u);
;             asm volatile("s_waitcnt vmcnt(0)" ::: "memory");
;         } else {
;             XB_SPIN(xb_ld(&bar[XB_XGEN(xq)]) == gen, bar);
;             __builtin_amdgcn_fence(__ATOMIC_ACQUIRE, "agent");
;             asm volatile("s_waitcnt vmcnt(0)" ::: "memory");
.LBB0_1005:
	s_or_b64 exec, exec, s[6:7]
	s_waitcnt vmcnt(0)
	s_waitcnt vmcnt(0)
.LBB0_1006:
	s_andn2_saveexec_b64 s[0:1], s[0:1]
	s_cbranch_execz .LBB0_1026
	s_mov_b64 s[0:1], exec
	buffer_wbl2 sc1
	s_waitcnt lgkmcnt(0)
	s_waitcnt vmcnt(0)
	buffer_inv sc1
	s_waitcnt vmcnt(0)
	v_mbcnt_lo_u32_b32 v1, s0, 0
	v_mbcnt_hi_u32_b32 v1, s1, v1
	v_cmp_eq_u32_e32 vcc, 0, v1
	s_and_saveexec_b64 s[6:7], vcc
	s_cbranch_execz .LBB0_1009
	s_bcnt1_i32_b64 s0, s[0:1]
	v_mov_b32_e32 v2, s0
	v_readlane_b32 s0, v254, 17
	v_readlane_b32 s1, v254, 18
	s_nop 4
	global_atomic_add v2, v81, v2, s[0:1] sc0

; __device__ __forceinline__ unsigned xb_ld(unsigned* p)              { return __hip_atomic_load(p, __ATOMIC_RELAXED, __HIP_MEMORY_SCOPE_AGENT); }
; __device__ __forceinline__ unsigned xb_add(unsigned* p, unsigned v) { return __hip_atomic_fetch_add(p, v, __ATOMIC_RELAXED, __HIP_MEMORY_SCOPE_AGENT); }
; #define XB_SPIN(cond, bar) do { unsigned _sp = 0; while (cond) { __builtin_amdgcn_s_sleep(1); \
;     if ((++_sp & 255u) == 0u) { if (xb_ld(&(bar)[XB_TMO])) break; if (_sp > XB_SPIN_CAP) { atomicAdd(&(bar)[XB_TMO], 1u); break; } } } } while (0)
; __device__ __forceinline__ void xcd_barrier(const XcdBarrier& b, int tid  ) {
;     ...
;             else XB_SPIN(xb_ld(&bar[XB_TOPGEN]) == tg, bar);
;             __builtin_amdgcn_fence(__ATOMIC_ACQUIRE, "agent");
;             xb_add(&bar[XB_XGEN(xq)], 1u);
;             asm volatile("s_waitcnt vmcnt(0)" ::: "memory");
.LBB0_1023:
	s_or_b64 exec, exec, s[0:1]
	s_mov_b64 s[0:1], exec
	v_mbcnt_lo_u32_b32 v0, s0, 0
	v_mbcnt_hi_u32_b32 v0, s1, v0
	v_cmp_eq_u32_e32 vcc, 0, v0
	s_waitcnt vmcnt(0)
	s_and_saveexec_b64 s[6:7], vcc
	s_cbranch_execz .LBB0_1025
	s_add_i32 s62, s21, 0x900
	s_lshl_b64 s[8:9], s[62:63], 2
	s_add_u32 s8, s64, s8
	s_addc_u32 s9, s65, s9
	s_bcnt1_i32_b64 s0, s[0:1]
	v_mov_b32_e32 v0, s0
	global_atomic_add v81, v0, s[8:9]

; __device__ __forceinline__ unsigned xb_ld(unsigned* p)              { return __hip_atomic_load(p, __ATOMIC_RELAXED, __HIP_MEMORY_SCOPE_AGENT); }
; __device__ __forceinline__ unsigned xb_add(unsigned* p, unsigned v) { return __hip_atomic_fetch_add(p, v, __ATOMIC_RELAXED, __HIP_MEMORY_SCOPE_AGENT); }
; #define XB_SPIN(cond, bar) do { unsigned _sp = 0; while (cond) { __builtin_amdgcn_s_sleep(1); \
;     if ((++_sp & 255u) == 0u) { if (xb_ld(&(bar)[XB_TMO])) break; if (_sp > XB_SPIN_CAP) { atomicAdd(&(bar)[XB_TMO], 1u); break; } } } } while (0)
; __device__ __forceinline__ void xcd_barrier(const XcdBarrier& b, int tid  ) {
;     asm volatile("s_waitcnt vmcnt(0)" ::: "memory");
;     __syncthreads();
;     if (tid == 0) {
;         unsigned* bar = b.bar; unsigned xq = b.x; asm volatile("" : "+s"(xq));
;         __builtin_amdgcn_s_waitcnt(0);
;         unsigned nloc = b.st[0], nx = b.st[1];
;         if (nloc == 0u) { xcd_barrier_complete(bar, xq, nloc, nx); b.st[0] = nloc; b.st[1] = nx; }
;         const unsigned old = xb_add(&bar[XB_XSUB(xq)], 1u);
;         const unsigned gen = old / nloc;
;         if (old + 1u == (gen + 1u) * nloc) {
;             __builtin_amdgcn_fence(__ATOMIC_RELEASE, "agent");
;             asm volatile("s_waitcnt vmcnt(0)" ::: "memory");
;             const unsigned og = xb_add(&bar[XB_TOP], 1u);
;             const unsigned tg = og / nx;
;             if (og + 1u == (tg + 1u) * nx) xb_add(&bar[XB_TOPGEN], 1u);
;             else XB_SPIN(xb_ld(&bar[XB_TOPGEN]) == tg, bar);
;             __builtin_amdgcn_fence(__ATOMIC_ACQUIRE, "agent");
;             xb_add(&bar[XB_XGEN(xq)], 1u);
;             asm volatile("s_waitcnt vmcnt(0)" ::: "memory");
;         } else {
;             XB_SPIN(xb_ld(&bar[XB_XGEN(xq)]) == gen, bar);
.LBB0_1217:
	s_or_b64 exec, exec, s[4:5]
	v_cvt_f32_u32_e32 v4, v2
	s_waitcnt vmcnt(0)
	v_readfirstlane_b32 s0, v3
	v_sub_u32_e32 v3, 0, v2
	v_rcp_iflag_f32_e32 v4, v4
	v_add_u32_e32 v5, s0, v1
	v_mul_f32_e32 v4, 0x4f7ffffe, v4
	v_cvt_u32_f32_e32 v4, v4
	v_mul_lo_u32 v1, v3, v4
	v_mul_hi_u32 v1, v4, v1
	v_add_u32_e32 v1, v4, v1
	v_mul_hi_u32 v1, v5, v1
	v_mul_lo_u32 v3, v1, v2
	v_sub_u32_e32 v3, v5, v3
	v_add_u32_e32 v4, 1, v1
	v_cmp_ge_u32_e32 vcc, v3, v2
	s_nop 1
	v_cndmask_b32_e32 v1, v1, v4, vcc
	v_sub_u32_e32 v4, v3, v2
	v_cndmask_b32_e32 v3, v3, v4, vcc
	v_add_u32_e32 v4, 1, v1
	v_cmp_ge_u32_e32 vcc, v3, v2
	v_add_u32_e32 v3, 1, v5
	s_nop 0
	v_cndmask_b32_e32 v1, v1, v4, vcc
	v_mul_lo_u32 v4, v2, v1
	v_add_u32_e32 v2, v4, v2
	v_cmp_ne_u32_e32 vcc, v3, v2
	s_and_saveexec_b64 s[0:1], vcc
	s_xor_b64 s[0:1], exec, s[0:1]
	s_cbranch_execz .LBB0_1231
	buffer_inv sc1
	s_movk_i32 s62, 0xd40
	s_lshl_b64 s[4:5], s[62:63], 2
	s_add_u32 s6, s64, s4
	s_addc_u32 s7, s65, s5
	s_waitcnt lgkmcnt(0)
	global_load_dword v0, v81, s[6:7] sc1
	s_waitcnt vmcnt(0)
	v_cmp_eq_u32_e32 vcc, v0, v1
	s_and_saveexec_b64 s[4:5], vcc
	s_cbranch_execz .LBB0_1230
	s_mov_b32 s19, 1
	s_mov_b64 s[8:9], 0
	s_branch .LBB0_1221

; __device__ __forceinline__ unsigned xb_ld(unsigned* p)              { return __hip_atomic_load(p, __ATOMIC_RELAXED, __HIP_MEMORY_SCOPE_AGENT); }
; __device__ __forceinline__ unsigned xb_add(unsigned* p, unsigned v) { return __hip_atomic_fetch_add(p, v, __ATOMIC_RELAXED, __HIP_MEMORY_SCOPE_AGENT); }
; #define XB_SPIN(cond, bar) do { unsigned _sp = 0; while (cond) { __builtin_amdgcn_s_sleep(1); \
;     if ((++_sp & 255u) == 0u) { if (xb_ld(&(bar)[XB_TMO])) break; if (_sp > XB_SPIN_CAP) { atomicAdd(&(bar)[XB_TMO], 1u); break; } } } } while (0)
; __device__ __forceinline__ void xcd_barrier(const XcdBarrier& b, int tid  ) {
;     ...
;             else XB_SPIN(xb_ld(&bar[XB_TOPGEN]) == tg, bar);
;             __builtin_amdgcn_fence(__ATOMIC_ACQUIRE, "agent");
;             xb_add(&bar[XB_XGEN(xq)], 1u);
;             asm volatile("s_waitcnt vmcnt(0)" ::: "memory");
.LBB0_1248:
	s_or_b64 exec, exec, s[0:1]
	s_mov_b64 s[0:1], exec
	v_mbcnt_lo_u32_b32 v0, s0, 0
	v_mbcnt_hi_u32_b32 v0, s1, v0
	v_cmp_eq_u32_e32 vcc, 0, v0
	s_waitcnt vmcnt(0)
	s_and_saveexec_b64 s[4:5], vcc
	s_cbranch_execz .LBB0_1250
	s_add_i32 s62, s18, 0x900
	s_lshl_b64 s[6:7], s[62:63], 2
	s_add_u32 s6, s64, s6
	s_addc_u32 s7, s65, s7
	s_bcnt1_i32_b64 s0, s[0:1]
	v_mov_b32_e32 v0, s0
	global_atomic_add v81, v0, s[6:7]

; __device__ __forceinline__ unsigned xb_add(unsigned* p, unsigned v) { return __hip_atomic_fetch_add(p, v, __ATOMIC_RELAXED, __HIP_MEMORY_SCOPE_AGENT); }
; __device__ __forceinline__ void xcd_barrier(const XcdBarrier& b, int tid  ) {
;     ...
;         if (old + 1u == (gen + 1u) * nloc) {
;             __builtin_amdgcn_fence(__ATOMIC_RELEASE, "agent");
;             asm volatile("s_waitcnt vmcnt(0)" ::: "memory");
;             const unsigned og = xb_add(&bar[XB_TOP], 1u);
;             const unsigned tg = og / nx;
;             if (og + 1u == (tg + 1u) * nx) xb_add(&bar[XB_TOPGEN], 1u);
.LBB0_1337:
	s_mov_b64 s[0:1], exec
	buffer_wbl2 sc1
	s_waitcnt lgkmcnt(0)
	s_waitcnt vmcnt(0)
	buffer_inv sc1
	s_waitcnt vmcnt(0)
	v_mbcnt_lo_u32_b32 v1, s0, 0
	v_mbcnt_hi_u32_b32 v1, s1, v1
	v_cmp_eq_u32_e32 vcc, 0, v1
	s_and_saveexec_b64 s[4:5], vcc
	s_cbranch_execz .LBB0_1339
	s_bcnt1_i32_b64 s0, s[0:1]
	v_mov_b32_e32 v2, s0
	v_readlane_b32 s0, v254, 17
	v_readlane_b32 s1, v254, 18
	s_nop 4
	global_atomic_add v2, v81, v2, s[0:1] sc0

; __device__ __forceinline__ unsigned xb_ld(unsigned* p)              { return __hip_atomic_load(p, __ATOMIC_RELAXED, __HIP_MEMORY_SCOPE_AGENT); }
; __device__ __forceinline__ unsigned xb_add(unsigned* p, unsigned v) { return __hip_atomic_fetch_add(p, v, __ATOMIC_RELAXED, __HIP_MEMORY_SCOPE_AGENT); }
; #define XB_SPIN(cond, bar) do { unsigned _sp = 0; while (cond) { __builtin_amdgcn_s_sleep(1); \
;     if ((++_sp & 255u) == 0u) { if (xb_ld(&(bar)[XB_TMO])) break; if (_sp > XB_SPIN_CAP) { atomicAdd(&(bar)[XB_TMO], 1u); break; } } } } while (0)
; __device__ __forceinline__ void xcd_barrier(const XcdBarrier& b, int tid  ) {
;     ...
;             else XB_SPIN(xb_ld(&bar[XB_TOPGEN]) == tg, bar);
;             __builtin_amdgcn_fence(__ATOMIC_ACQUIRE, "agent");
;             xb_add(&bar[XB_XGEN(xq)], 1u);
;             asm volatile("s_waitcnt vmcnt(0)" ::: "memory");
.LBB0_1353:
	s_or_b64 exec, exec, s[0:1]
	s_mov_b64 s[0:1], exec
	v_mbcnt_lo_u32_b32 v0, s0, 0
	v_mbcnt_hi_u32_b32 v0, s1, v0
	v_cmp_eq_u32_e32 vcc, 0, v0
	s_waitcnt vmcnt(0)
	s_and_saveexec_b64 s[4:5], vcc
	s_cbranch_execnz .LBB0_1354
	s_getpc_b64 s[98:99]
